# speedup vs baseline: 1.0309x; 1.0309x over previous
_Z7dog_finPKfS0_Pf:
	s_load_dwordx4 s[4:7], s[0:1], 0x0
	s_load_dwordx2 s[8:9], s[0:1], 0x10
	s_and_b32 s3, s2, 7
	s_lshl_b32 s3, s3, 3
	s_lshr_b32 s10, s2, 3
	s_add_i32 s3, s3, s10
	v_lshlrev_b32_e32 v1, 2, v0
	s_lshl_b32 s3, s3, 10
	v_add_u32_e32 v2, s3, v1
	s_mov_b32 s10, 0x10000
	v_add_u32_e32 v3, s10, v2
	v_add_u32_e32 v4, s10, v3
	v_add_u32_e32 v5, s10, v4
	s_waitcnt lgkmcnt(0)
	global_load_dword v12, v2, s[4:5]
	global_load_dword v14, v3, s[4:5]
	global_load_dword v13, v4, s[4:5]
	global_load_dword v15, v5, s[4:5]
	global_load_dword v6, v1, s[6:7]
	s_waitcnt vmcnt(1)
	v_pk_add_f32 v[8:9], v[12:13], v[14:15]
	s_nop 0
	v_add_f32_e32 v8, v8, v9
	s_waitcnt vmcnt(0)
	v_add_f32_e32 v6, v6, v8
	global_store_dword v2, v6, s[8:9]
	s_endpgm
